# v048 + P16 (layer-1 gate/up GEMM) epilogue: token-scale loads of rows 2..7 hoisted to the epilogue start with counted waits, as done for P6
# speedup vs baseline: 1.0026x; 1.0026x over previous
.LBB0_3083:
	s_lshl_b32 s1, s26, 2
	s_add_i32 s1, s1, 0
	s_add_i32 s1, s1, 0x20480
	v_mov_b32_e32 v74, s1
	s_ashr_i32 s27, s26, 31
	ds_read_b32 v74, v74
	s_lshl_b64 s[22:23], s[26:27], 13
	s_add_u32 s28, s47, s22
	s_addc_u32 s29, s48, s23
	s_add_u32 s1, s45, s22
	s_addc_u32 s19, s46, s23
	s_lshl_b32 s22, s24, 8
	v_lshl_or_b32 v201, s24, 7, v170
	s_waitcnt lgkmcnt(0)
	v_sub_u32_e32 v74, s57, v74
	s_ashr_i32 s23, s22, 31
	v_lshl_add_u32 v172, v74, 8, v178
	v_lshlrev_b32_e32 v74, 1, v201
	s_lshl_b64 s[22:23], s[22:23], 2
	v_ashrrev_i32_e32 v75, 31, v74
	s_add_u32 s22, s1, s22
	v_lshl_add_u64 v[82:83], v[74:75], 2, s[28:29]
	s_addc_u32 s23, s19, s23
	v_lshlrev_b32_e32 v110, 2, v170
	global_load_dwordx4 v[98:101], v[82:83], off offset:16
	global_load_dwordx4 v[114:117], v[82:83], off
	global_load_dwordx4 v[74:77], v[82:83], off offset:48
	global_load_dwordx4 v[90:93], v[82:83], off offset:32
	s_nop 0
	global_load_dwordx4 v[82:85], v110, s[22:23] offset:16
	global_load_dwordx4 v[106:109], v110, s[22:23]
	global_load_dwordx4 v[86:89], v110, s[22:23] offset:528
	s_nop 0
	global_load_dwordx4 v[110:113], v110, s[22:23] offset:512
	s_lshl_b64 s[22:23], s[26:27], 18
	s_add_u32 s22, s66, s22
	v_ashrrev_i32_e32 v173, 31, v172
	s_addc_u32 s23, s67, s23
	v_lshl_add_u64 v[172:173], v[172:173], 2, s[22:23]
	global_load_dword v200, v[172:173], off
	global_load_dword v206, v[172:173], off offset:64
	global_load_dword v220, v[172:173], off offset:128
	global_load_dword v222, v[172:173], off offset:192
	global_load_dword v224, v[172:173], off offset:512
	global_load_dword v226, v[172:173], off offset:576
	global_load_dword v228, v[172:173], off offset:640
	global_load_dword v230, v[172:173], off offset:704
	v_cvt_f32_i32_e32 v161, v161
	v_cvt_f32_i32_e32 v160, v160
	v_cvt_f32_i32_e32 v159, v159
	v_cvt_f32_i32_e32 v158, v158
	v_cvt_f32_i32_e32 v202, v150
	v_cvt_f32_i32_e32 v203, v151
	v_cvt_f32_i32_e32 v153, v153
	v_cvt_f32_i32_e32 v152, v152
	v_cvt_f32_i32_e32 v157, v157
	v_cvt_f32_i32_e32 v156, v156
	v_cvt_f32_i32_e32 v155, v155
	v_cvt_f32_i32_e32 v154, v154
	v_cvt_f32_i32_e32 v205, v147
	v_cvt_f32_i32_e32 v204, v146
	v_cvt_f32_i32_e32 v149, v149
	v_cvt_f32_i32_e32 v148, v148
	v_cvt_f32_i32_e32 v143, v143
	v_cvt_f32_i32_e32 v142, v142
	v_cvt_f32_i32_e32 v139, v139
	v_cvt_f32_i32_e32 v138, v138
	v_cvt_f32_i32_e32 v135, v135
	v_cvt_f32_i32_e32 v134, v134
	v_cvt_f32_i32_e32 v141, v141
	v_cvt_f32_i32_e32 v140, v140
	v_cvt_f32_i32_e32 v131, v131
	v_cvt_f32_i32_e32 v130, v130
	v_cvt_f32_i32_e32 v137, v137
	v_cvt_f32_i32_e32 v136, v136
	v_cvt_f32_i32_e32 v133, v133
	v_cvt_f32_i32_e32 v132, v132
	v_lshl_add_u32 v169, s57, 8, v178
	v_sub_u32_e32 v146, v201, v179
	v_ashrrev_i32_e32 v147, 31, v146
	v_cvt_f32_i32_e32 v127, v127
	v_cvt_f32_i32_e32 v126, v126
	v_cvt_f32_i32_e32 v129, v129
	v_cvt_f32_i32_e32 v128, v128
	v_cvt_f32_i32_e32 v123, v123
	v_cvt_f32_i32_e32 v122, v122
	v_cvt_f32_i32_e32 v125, v125
	v_cvt_f32_i32_e32 v124, v124
	v_cvt_f32_i32_e32 v119, v119
	v_cvt_f32_i32_e32 v118, v118
	v_cvt_f32_i32_e32 v121, v121
	v_cvt_f32_i32_e32 v120, v120
	v_cvt_f32_i32_e32 v103, v103
	v_cvt_f32_i32_e32 v102, v102
	v_cvt_f32_i32_e32 v105, v105
	v_cvt_f32_i32_e32 v104, v104
	v_cvt_f32_i32_e32 v95, v95
	v_cvt_f32_i32_e32 v94, v94
	v_cvt_f32_i32_e32 v79, v79
	v_cvt_f32_i32_e32 v78, v78
	v_cvt_f32_i32_e32 v97, v97
	v_cvt_f32_i32_e32 v96, v96
	v_cvt_f32_i32_e32 v71, v71
	v_cvt_f32_i32_e32 v70, v70
	v_cvt_f32_i32_e32 v81, v81
	v_cvt_f32_i32_e32 v80, v80
	v_cvt_f32_i32_e32 v67, v67
	v_cvt_f32_i32_e32 v66, v66
	v_cvt_f32_i32_e32 v73, v73
	v_cvt_f32_i32_e32 v72, v72
	v_cvt_f32_i32_e32 v69, v69
	v_cvt_f32_i32_e32 v68, v68
	v_cvt_f32_i32_e32 v65, v65
	v_cvt_f32_i32_e32 v64, v64
	v_cvt_f32_i32_e32 v59, v59
	s_waitcnt vmcnt(6)
	v_mov_b32_e32 v150, v99
	v_mov_b32_e32 v99, v100
	v_pk_mul_f32 v[160:161], v[108:109], v[160:161]
	v_mov_b32_e32 v210, v75
	v_mov_b32_e32 v211, v77
	v_mov_b32_e32 v212, v91
	v_mov_b32_e32 v213, v93
	v_mov_b32_e32 v91, v92
	v_pk_add_f32 v[92:93], v[210:211], 1.0 op_sel_hi:[1,0]
	v_mov_b32_e32 v208, v115
	v_pk_fma_f32 v[160:161], v[160:161], v[200:201], v[98:99] op_sel_hi:[1,0,1]
	v_mov_b32_e32 v115, v116
	v_min_f32_e32 v160, 0x40e00000, v160
	v_min_f32_e32 v161, 0x40e00000, v161
	v_pk_mul_f32 v[210:211], v[160:161], s[12:13] op_sel_hi:[1,0]
	v_pk_mul_f32 v[158:159], v[106:107], v[158:159]
	v_exp_f32_e32 v210, v210
	v_exp_f32_e32 v211, v211
	v_pk_fma_f32 v[158:159], v[158:159], v[200:201], v[114:115] op_sel_hi:[1,0,1]
	v_mov_b32_e32 v151, v101
	v_mov_b32_e32 v209, v117
	v_pk_mul_f32 v[202:203], v[82:83], v[202:203]
	v_min_f32_e32 v158, 0x40e00000, v158
	v_min_f32_e32 v159, 0x40e00000, v159
	v_mov_b32_e32 v75, v76
	v_pk_mul_f32 v[76:77], v[84:85], v[152:153]
	v_pk_add_f32 v[116:117], v[150:151], 1.0 op_sel_hi:[1,0]
	v_pk_add_f32 v[150:151], v[208:209], 1.0 op_sel_hi:[1,0]
	v_pk_fma_f32 v[202:203], v[202:203], v[200:201], v[90:91] op_sel_hi:[1,0,1]
	v_pk_mul_f32 v[208:209], v[158:159], s[12:13] op_sel_hi:[1,0]
	v_pk_fma_f32 v[76:77], v[76:77], v[200:201], v[74:75] op_sel_hi:[1,0,1]
	v_min_f32_e32 v202, 0x40e00000, v202
	v_exp_f32_e32 v208, v208
	v_exp_f32_e32 v209, v209
	v_min_f32_e32 v203, 0x40e00000, v203
	v_pk_fma_f32 v[210:211], v[210:211], s[14:15], s[14:15] op_sel_hi:[1,0,0]
	v_min_f32_e32 v76, 0x40e00000, v76
	v_min_f32_e32 v77, 0x40e00000, v77
	v_pk_add_f32 v[100:101], v[212:213], 1.0 op_sel_hi:[1,0]
	v_pk_mul_f32 v[212:213], v[202:203], s[12:13] op_sel_hi:[1,0]
	v_rcp_f32_e32 v210, v210
	v_rcp_f32_e32 v211, v211
	v_pk_mul_f32 v[152:153], v[76:77], s[12:13] op_sel_hi:[1,0]
	v_exp_f32_e32 v212, v212
	v_exp_f32_e32 v213, v213
	v_exp_f32_e32 v152, v152
	v_exp_f32_e32 v153, v153
	v_pk_mul_f32 v[156:157], v[112:113], v[156:157]
	v_pk_fma_f32 v[208:209], v[208:209], s[14:15], s[14:15] op_sel_hi:[1,0,0]
	v_pk_fma_f32 v[156:157], v[156:157], v[200:201], v[116:117] op_sel_hi:[1,0,1]
	v_rcp_f32_e32 v208, v208
	v_med3_f32 v156, v156, s55, v199
	v_med3_f32 v157, v157, s55, v199
	v_rcp_f32_e32 v209, v209
	v_pk_mul_f32 v[160:161], v[160:161], v[210:211]
	v_pk_fma_f32 v[152:153], v[152:153], s[14:15], s[14:15] op_sel_hi:[1,0,0]
	v_pk_mul_f32 v[156:157], v[156:157], v[160:161]
	v_pk_fma_f32 v[160:161], v[212:213], s[14:15], s[14:15] op_sel_hi:[1,0,0]
	v_pk_mul_f32 v[154:155], v[110:111], v[154:155]
	v_rcp_f32_e32 v160, v160
	v_rcp_f32_e32 v161, v161
	v_rcp_f32_e32 v152, v152
	v_rcp_f32_e32 v153, v153
	v_pk_fma_f32 v[154:155], v[154:155], v[200:201], v[150:151] op_sel_hi:[1,0,1]
	v_pk_mul_f32 v[204:205], v[86:87], v[204:205]
	v_med3_f32 v154, v154, s55, v199
	v_med3_f32 v155, v155, s55, v199
	v_pk_mul_f32 v[158:159], v[158:159], v[208:209]
	v_pk_mul_f32 v[148:149], v[88:89], v[148:149]
	v_pk_mul_f32 v[142:143], v[106:107], v[142:143]
	v_pk_mul_f32 v[154:155], v[154:155], v[158:159]
	v_pk_fma_f32 v[158:159], v[204:205], v[200:201], v[100:101] op_sel_hi:[1,0,1]
	v_pk_fma_f32 v[148:149], v[148:149], v[200:201], v[92:93] op_sel_hi:[1,0,1]
	v_pk_fma_f32 v[142:143], v[142:143], v[206:207], v[114:115] op_sel_hi:[1,0,1]
	v_med3_f32 v158, v158, s55, v199
	v_med3_f32 v159, v159, s55, v199
	v_pk_mul_f32 v[160:161], v[202:203], v[160:161]
	v_med3_f32 v148, v148, s55, v199
	v_med3_f32 v149, v149, s55, v199
	v_pk_mul_f32 v[76:77], v[76:77], v[152:153]
	v_min_f32_e32 v142, 0x40e00000, v142
	v_min_f32_e32 v143, 0x40e00000, v143
	v_pk_mul_f32 v[158:159], v[158:159], v[160:161]
	v_pk_mul_f32 v[76:77], v[148:149], v[76:77]
	s_nop 0
	v_pk_mul_f32 v[148:149], v[142:143], s[12:13] op_sel_hi:[1,0]
	v_cvt_pk_fp8_f32 v153, v158, v159
	v_exp_f32_e32 v148, v148
	v_exp_f32_e32 v149, v149
	v_pk_mul_f32 v[134:135], v[82:83], v[134:135]
	v_cvt_pk_fp8_f32 v153, v76, v77 op_sel:[0,0,1]
	v_pk_mul_f32 v[76:77], v[110:111], v[138:139]
	v_pk_fma_f32 v[138:139], v[148:149], s[14:15], s[14:15] op_sel_hi:[1,0,0]
	v_pk_fma_f32 v[76:77], v[76:77], v[206:207], v[150:151] op_sel_hi:[1,0,1]
	v_rcp_f32_e32 v138, v138
	v_rcp_f32_e32 v139, v139
	v_med3_f32 v76, v76, s55, v199
	v_med3_f32 v77, v77, s55, v199
	v_pk_fma_f32 v[134:135], v[134:135], v[206:207], v[90:91] op_sel_hi:[1,0,1]
	v_pk_mul_f32 v[138:139], v[142:143], v[138:139]
	v_cvt_f32_i32_e32 v143, v145
	v_cvt_f32_i32_e32 v142, v144
	v_pk_mul_f32 v[76:77], v[76:77], v[138:139]
	v_min_f32_e32 v134, 0x40e00000, v134
	v_min_f32_e32 v135, 0x40e00000, v135
	v_pk_mul_f32 v[138:139], v[108:109], v[142:143]
	v_pk_mul_f32 v[144:145], v[134:135], s[12:13] op_sel_hi:[1,0]
	v_pk_fma_f32 v[138:139], v[138:139], v[206:207], v[98:99] op_sel_hi:[1,0,1]
	v_exp_f32_e32 v144, v144
	v_min_f32_e32 v138, 0x40e00000, v138
	v_min_f32_e32 v139, 0x40e00000, v139
	v_pk_mul_f32 v[142:143], v[138:139], s[12:13] op_sel_hi:[1,0]
	v_exp_f32_e32 v145, v145
	v_exp_f32_e32 v142, v142
	v_exp_f32_e32 v143, v143
	v_pk_mul_f32 v[140:141], v[112:113], v[140:141]
	v_pk_mul_f32 v[130:131], v[86:87], v[130:131]
	v_pk_fma_f32 v[140:141], v[140:141], v[206:207], v[116:117] op_sel_hi:[1,0,1]
	v_pk_fma_f32 v[142:143], v[142:143], s[14:15], s[14:15] op_sel_hi:[1,0,0]
	v_med3_f32 v140, v140, s55, v199
	v_rcp_f32_e32 v142, v142
	v_rcp_f32_e32 v143, v143
	v_med3_f32 v141, v141, s55, v199
	v_pk_fma_f32 v[130:131], v[130:131], v[206:207], v[100:101] op_sel_hi:[1,0,1]
	s_nop 0
	v_pk_mul_f32 v[138:139], v[138:139], v[142:143]
	v_med3_f32 v130, v130, s55, v199
	v_pk_mul_f32 v[138:139], v[140:141], v[138:139]
	v_pk_fma_f32 v[140:141], v[144:145], s[14:15], s[14:15] op_sel_hi:[1,0,0]
	v_med3_f32 v131, v131, s55, v199
	v_rcp_f32_e32 v140, v140
	v_rcp_f32_e32 v141, v141
	v_cvt_pk_fp8_f32 v152, v154, v155
	s_nop 0
	s_nop 0
	v_pk_mul_f32 v[134:135], v[134:135], v[140:141]
	v_pk_mul_f32 v[132:133], v[88:89], v[132:133]
	v_pk_mul_f32 v[130:131], v[130:131], v[134:135]
	v_pk_mul_f32 v[134:135], v[84:85], v[136:137]
	v_cvt_pk_fp8_f32 v154, v76, v77
	v_pk_fma_f32 v[134:135], v[134:135], v[206:207], v[74:75] op_sel_hi:[1,0,1]
	v_cvt_pk_fp8_f32 v155, v130, v131
	v_min_f32_e32 v134, 0x40e00000, v134
	v_min_f32_e32 v135, 0x40e00000, v135
	v_pk_mul_f32 v[136:137], v[134:135], s[12:13] op_sel_hi:[1,0]
	v_pk_fma_f32 v[132:133], v[132:133], v[206:207], v[92:93] op_sel_hi:[1,0,1]
	v_exp_f32_e32 v136, v136
	v_exp_f32_e32 v137, v137
	v_med3_f32 v132, v132, s55, v199
	v_med3_f32 v133, v133, s55, v199
	v_cvt_pk_fp8_f32 v152, v156, v157 op_sel:[0,0,1]
	v_pk_fma_f32 v[136:137], v[136:137], s[14:15], s[14:15] op_sel_hi:[1,0,0]
	v_cvt_pk_fp8_f32 v154, v138, v139 op_sel:[0,0,1]
	v_rcp_f32_e32 v136, v136
	v_rcp_f32_e32 v137, v137
	v_pk_mul_f32 v[126:127], v[106:107], v[126:127]
	v_permlane16_swap_b32_e32 v152, v154
	v_pk_mul_f32 v[76:77], v[134:135], v[136:137]
	v_pk_mul_f32 v[128:129], v[108:109], v[128:129]
	v_pk_mul_f32 v[76:77], v[132:133], v[76:77]
	v_pk_mul_f32 v[122:123], v[110:111], v[122:123]
	v_cvt_pk_fp8_f32 v155, v76, v77 op_sel:[0,0,1]
	v_or_b32_e32 v76, v169, v180
	v_ashrrev_i32_e32 v77, 31, v76
	v_lshlrev_b64 v[76:77], 10, v[76:77]
	v_lshl_add_u64 v[76:77], s[94:95], 0, v[76:77]
	v_permlane16_swap_b32_e32 v153, v155
	v_lshl_add_u64 v[76:77], v[76:77], 0, v[146:147]
	global_store_dwordx4 v[76:77], v[152:155], off
	s_nop 0
	v_pk_mul_f32 v[124:125], v[112:113], v[124:125]
	s_nop 0
	v_pk_mul_f32 v[118:119], v[82:83], v[118:119]
	v_pk_mul_f32 v[120:121], v[84:85], v[120:121]
	v_pk_mul_f32 v[102:103], v[86:87], v[102:103]
	v_pk_mul_f32 v[104:105], v[88:89], v[104:105]
	v_pk_mul_f32 v[94:95], v[106:107], v[94:95]
	v_pk_mul_f32 v[78:79], v[110:111], v[78:79]
	v_pk_mul_f32 v[70:71], v[82:83], v[70:71]
	v_pk_mul_f32 v[80:81], v[112:113], v[80:81]
	v_pk_mul_f32 v[66:67], v[86:87], v[66:67]
	v_pk_mul_f32 v[68:69], v[88:89], v[68:69]
	v_pk_mul_f32 v[64:65], v[108:109], v[64:65]
	v_cvt_f32_i32_e32 v58, v58
	v_cvt_f32_i32_e32 v61, v61
	v_cvt_f32_i32_e32 v60, v60
	v_cvt_f32_i32_e32 v55, v55
	v_pk_mul_f32 v[58:59], v[110:111], v[58:59]
	v_cvt_f32_i32_e32 v54, v54
	v_pk_mul_f32 v[60:61], v[112:113], v[60:61]
	v_cvt_f32_i32_e32 v57, v57
	v_cvt_f32_i32_e32 v56, v56
	v_pk_mul_f32 v[54:55], v[82:83], v[54:55]
	v_cvt_f32_i32_e32 v51, v51
	v_cvt_f32_i32_e32 v50, v50
	v_pk_mul_f32 v[56:57], v[84:85], v[56:57]
	v_cvt_f32_i32_e32 v53, v53
	v_cvt_f32_i32_e32 v52, v52
	v_pk_mul_f32 v[50:51], v[86:87], v[50:51]
	v_cvt_f32_i32_e32 v47, v47
	v_cvt_f32_i32_e32 v46, v46
	v_cvt_f32_i32_e32 v43, v43
	v_cvt_f32_i32_e32 v42, v42
	v_cvt_f32_i32_e32 v49, v49
	v_pk_mul_f32 v[46:47], v[106:107], v[46:47]
	v_cvt_f32_i32_e32 v48, v48
	v_pk_mul_f32 v[42:43], v[110:111], v[42:43]
	v_cvt_f32_i32_e32 v39, v39
	v_cvt_f32_i32_e32 v38, v38
	v_cvt_f32_i32_e32 v45, v45
	v_cvt_f32_i32_e32 v44, v44
	v_cvt_f32_i32_e32 v31, v31
	v_pk_mul_f32 v[38:39], v[82:83], v[38:39]
	v_cvt_f32_i32_e32 v30, v30
	v_pk_mul_f32 v[44:45], v[112:113], v[44:45]
	v_cvt_f32_i32_e32 v41, v41
	v_cvt_f32_i32_e32 v40, v40
	v_pk_mul_f32 v[30:31], v[86:87], v[30:31]
	v_cvt_f32_i32_e32 v33, v33
	v_cvt_f32_i32_e32 v32, v32
	v_cvt_f32_i32_e32 v23, v23
	v_cvt_f32_i32_e32 v22, v22
	v_cvt_f32_i32_e32 v25, v25
	v_pk_mul_f32 v[32:33], v[88:89], v[32:33]
	v_cvt_f32_i32_e32 v24, v24
	v_pk_mul_f32 v[22:23], v[106:107], v[22:23]
	v_cvt_f32_i32_e32 v37, v37
	v_cvt_f32_i32_e32 v36, v36
	v_pk_mul_f32 v[24:25], v[108:109], v[24:25]
	v_cvt_f32_i32_e32 v15, v15
	v_cvt_f32_i32_e32 v14, v14
	v_cvt_f32_i32_e32 v17, v17
	v_cvt_f32_i32_e32 v16, v16
	v_cvt_f32_i32_e32 v27, v27
	v_pk_mul_f32 v[14:15], v[82:83], v[14:15]
	v_cvt_f32_i32_e32 v26, v26
	v_pk_mul_f32 v[16:17], v[84:85], v[16:17]
	v_cvt_f32_i32_e32 v29, v29
	v_cvt_f32_i32_e32 v28, v28
	v_pk_mul_f32 v[26:27], v[86:87], v[26:27]
	v_cvt_f32_i32_e32 v7, v7
	v_cvt_f32_i32_e32 v6, v6
	v_cvt_f32_i32_e32 v19, v19
	v_cvt_f32_i32_e32 v18, v18
	v_cvt_f32_i32_e32 v9, v9
	v_pk_mul_f32 v[6:7], v[106:107], v[6:7]
	v_cvt_f32_i32_e32 v8, v8
	v_cvt_f32_i32_e32 v3, v3
	v_cvt_f32_i32_e32 v2, v2
	s_waitcnt vmcnt(6)
	v_pk_fma_f32 v[126:127], v[126:127], v[220:221], v[114:115] op_sel_hi:[1,0,1]
	v_pk_fma_f32 v[128:129], v[128:129], v[220:221], v[98:99] op_sel_hi:[1,0,1]
	v_min_f32_e32 v126, 0x40e00000, v126
	v_min_f32_e32 v127, 0x40e00000, v127
	v_pk_mul_f32 v[132:133], v[126:127], s[12:13] op_sel_hi:[1,0]
	v_min_f32_e32 v128, 0x40e00000, v128
	v_exp_f32_e32 v132, v132
	v_exp_f32_e32 v133, v133
	v_min_f32_e32 v129, 0x40e00000, v129
	v_pk_mul_f32 v[134:135], v[128:129], s[12:13] op_sel_hi:[1,0]
	v_pk_fma_f32 v[122:123], v[122:123], v[220:221], v[150:151] op_sel_hi:[1,0,1]
	v_pk_fma_f32 v[132:133], v[132:133], s[14:15], s[14:15] op_sel_hi:[1,0,0]
	v_exp_f32_e32 v134, v134
	v_rcp_f32_e32 v132, v132
	v_rcp_f32_e32 v133, v133
	v_exp_f32_e32 v135, v135
	v_med3_f32 v122, v122, s55, v199
	v_med3_f32 v123, v123, s55, v199
	v_pk_mul_f32 v[126:127], v[126:127], v[132:133]
	v_pk_fma_f32 v[124:125], v[124:125], v[220:221], v[116:117] op_sel_hi:[1,0,1]
	v_pk_mul_f32 v[122:123], v[122:123], v[126:127]
	v_pk_fma_f32 v[126:127], v[134:135], s[14:15], s[14:15] op_sel_hi:[1,0,0]
	v_pk_fma_f32 v[118:119], v[118:119], v[220:221], v[90:91] op_sel_hi:[1,0,1]
	v_rcp_f32_e32 v126, v126
	v_rcp_f32_e32 v127, v127
	v_med3_f32 v124, v124, s55, v199
	v_med3_f32 v125, v125, s55, v199
	v_min_f32_e32 v118, 0x40e00000, v118
	v_pk_mul_f32 v[126:127], v[128:129], v[126:127]
	v_min_f32_e32 v119, 0x40e00000, v119
	v_pk_mul_f32 v[124:125], v[124:125], v[126:127]
	v_pk_mul_f32 v[126:127], v[118:119], s[12:13] op_sel_hi:[1,0]
	v_pk_fma_f32 v[120:121], v[120:121], v[220:221], v[74:75] op_sel_hi:[1,0,1]
	v_exp_f32_e32 v126, v126
	v_exp_f32_e32 v127, v127
	v_min_f32_e32 v120, 0x40e00000, v120
	v_min_f32_e32 v121, 0x40e00000, v121
	v_pk_mul_f32 v[128:129], v[120:121], s[12:13] op_sel_hi:[1,0]
	v_pk_fma_f32 v[126:127], v[126:127], s[14:15], s[14:15] op_sel_hi:[1,0,0]
	v_exp_f32_e32 v128, v128
	v_rcp_f32_e32 v126, v126
	v_rcp_f32_e32 v127, v127
	v_exp_f32_e32 v129, v129
	v_pk_fma_f32 v[102:103], v[102:103], v[220:221], v[100:101] op_sel_hi:[1,0,1]
	v_pk_fma_f32 v[76:77], v[104:105], v[220:221], v[92:93] op_sel_hi:[1,0,1]
	v_med3_f32 v102, v102, s55, v199
	v_med3_f32 v103, v103, s55, v199
	v_pk_mul_f32 v[118:119], v[118:119], v[126:127]
	v_med3_f32 v76, v76, s55, v199
	v_pk_mul_f32 v[102:103], v[102:103], v[118:119]
	v_pk_fma_f32 v[118:119], v[128:129], s[14:15], s[14:15] op_sel_hi:[1,0,0]
	v_med3_f32 v77, v77, s55, v199
	v_rcp_f32_e32 v118, v118
	v_rcp_f32_e32 v119, v119
	s_waitcnt vmcnt(5)
	v_pk_fma_f32 v[94:95], v[94:95], v[222:223], v[114:115] op_sel_hi:[1,0,1]
	v_pk_fma_f32 v[78:79], v[78:79], v[222:223], v[150:151] op_sel_hi:[1,0,1]
	v_min_f32_e32 v94, 0x40e00000, v94
	v_pk_mul_f32 v[104:105], v[120:121], v[118:119]
	v_min_f32_e32 v95, 0x40e00000, v95
	v_pk_mul_f32 v[104:105], v[76:77], v[104:105]
	s_nop 0
	v_cvt_pk_fp8_f32 v77, v102, v103
	v_pk_mul_f32 v[102:103], v[94:95], s[12:13] op_sel_hi:[1,0]
	v_med3_f32 v78, v78, s55, v199
	v_exp_f32_e32 v102, v102
	v_exp_f32_e32 v103, v103
	v_med3_f32 v79, v79, s55, v199
	v_pk_fma_f32 v[70:71], v[70:71], v[222:223], v[90:91] op_sel_hi:[1,0,1]
	v_pk_fma_f32 v[80:81], v[80:81], v[222:223], v[116:117] op_sel_hi:[1,0,1]
	v_pk_fma_f32 v[102:103], v[102:103], s[14:15], s[14:15] op_sel_hi:[1,0,0]
	v_min_f32_e32 v70, 0x40e00000, v70
	v_rcp_f32_e32 v102, v102
	v_rcp_f32_e32 v103, v103
	v_min_f32_e32 v71, 0x40e00000, v71
	v_med3_f32 v80, v80, s55, v199
	v_med3_f32 v81, v81, s55, v199
	v_pk_mul_f32 v[94:95], v[94:95], v[102:103]
	v_pk_mul_f32 v[102:103], v[70:71], s[12:13] op_sel_hi:[1,0]
	v_pk_mul_f32 v[94:95], v[78:79], v[94:95]
	v_pk_mul_f32 v[78:79], v[108:109], v[96:97]
	v_exp_f32_e32 v102, v102
	v_pk_fma_f32 v[78:79], v[78:79], v[222:223], v[98:99] op_sel_hi:[1,0,1]
	v_exp_f32_e32 v103, v103
	v_min_f32_e32 v78, 0x40e00000, v78
	v_min_f32_e32 v79, 0x40e00000, v79
	v_pk_mul_f32 v[96:97], v[78:79], s[12:13] op_sel_hi:[1,0]
	v_pk_fma_f32 v[66:67], v[66:67], v[222:223], v[100:101] op_sel_hi:[1,0,1]
	v_exp_f32_e32 v96, v96
	v_exp_f32_e32 v97, v97
	v_med3_f32 v66, v66, s55, v199
	v_med3_f32 v67, v67, s55, v199
	s_nop 0
	v_pk_fma_f32 v[96:97], v[96:97], s[14:15], s[14:15] op_sel_hi:[1,0,0]
	v_cvt_pk_fp8_f32 v76, v122, v123
	v_rcp_f32_e32 v96, v96
	v_rcp_f32_e32 v97, v97
	v_pk_fma_f32 v[68:69], v[68:69], v[222:223], v[92:93] op_sel_hi:[1,0,1]
	v_cvt_pk_fp8_f32 v76, v124, v125 op_sel:[0,0,1]
	v_med3_f32 v68, v68, s55, v199
	v_pk_mul_f32 v[78:79], v[78:79], v[96:97]
	v_med3_f32 v69, v69, s55, v199
	v_pk_mul_f32 v[80:81], v[80:81], v[78:79]
	v_pk_fma_f32 v[78:79], v[102:103], s[14:15], s[14:15] op_sel_hi:[1,0,0]
	v_cvt_pk_fp8_f32 v77, v104, v105 op_sel:[0,0,1]
	v_rcp_f32_e32 v78, v78
	v_rcp_f32_e32 v79, v79
	v_pk_mul_f32 v[8:9], v[108:109], v[8:9]
	v_pk_mul_f32 v[2:3], v[82:83], v[2:3]
	v_cvt_f32_i32_e32 v11, v11
	v_pk_mul_f32 v[70:71], v[70:71], v[78:79]
	s_nop 0
	v_pk_mul_f32 v[66:67], v[66:67], v[70:71]
	v_pk_mul_f32 v[70:71], v[84:85], v[72:73]
	s_nop 0
	v_pk_fma_f32 v[70:71], v[70:71], v[222:223], v[74:75] op_sel_hi:[1,0,1]
	v_cvt_pk_fp8_f32 v78, v94, v95
	v_min_f32_e32 v70, 0x40e00000, v70
	v_min_f32_e32 v71, 0x40e00000, v71
	v_pk_mul_f32 v[72:73], v[70:71], s[12:13] op_sel_hi:[1,0]
	v_cvt_pk_fp8_f32 v79, v66, v67
	v_exp_f32_e32 v72, v72
	v_exp_f32_e32 v73, v73
	v_cvt_pk_fp8_f32 v78, v80, v81 op_sel:[0,0,1]
	v_cvt_f32_i32_e32 v10, v10
	v_cvt_f32_i32_e32 v5, v5
	v_pk_fma_f32 v[72:73], v[72:73], s[14:15], s[14:15] op_sel_hi:[1,0,0]
	v_permlane16_swap_b32_e32 v76, v78
	v_rcp_f32_e32 v72, v72
	v_rcp_f32_e32 v73, v73
	v_cvt_f32_i32_e32 v4, v4
	v_cvt_f32_i32_e32 v13, v13
	v_cvt_f32_i32_e32 v12, v12
	v_pk_mul_f32 v[66:67], v[70:71], v[72:73]
	v_pk_mul_f32 v[10:11], v[86:87], v[10:11]
	v_pk_mul_f32 v[66:67], v[68:69], v[66:67]
	v_cvt_f32_i32_e32 v69, v63
	v_cvt_pk_fp8_f32 v79, v66, v67 op_sel:[0,0,1]
	v_or_b32_e32 v66, v169, v181
	v_ashrrev_i32_e32 v67, 31, v66
	v_lshlrev_b64 v[66:67], 10, v[66:67]
	v_lshl_add_u64 v[66:67], s[94:95], 0, v[66:67]
	v_permlane16_swap_b32_e32 v77, v79
	v_lshl_add_u64 v[66:67], v[66:67], 0, v[146:147]
	global_store_dwordx4 v[66:67], v[76:79], off
	s_nop 0
	v_cvt_f32_i32_e32 v68, v62
	s_nop 0
	v_add_u32_e32 v62, 0x80, v169
	v_pk_mul_f32 v[4:5], v[84:85], v[4:5]
	v_pk_mul_f32 v[68:69], v[106:107], v[68:69]
	s_and_b64 vcc, exec, s[2:3]
	s_mov_b64 s[2:3], -1
	s_mov_b32 s59, s62
	s_mov_b32 s58, s63
	s_waitcnt vmcnt(5)
	v_pk_fma_f32 v[68:69], v[68:69], v[224:225], v[114:115] op_sel_hi:[1,0,1]
	s_nop 0
	v_min_f32_e32 v68, 0x40e00000, v68
	v_min_f32_e32 v69, 0x40e00000, v69
	v_pk_mul_f32 v[72:73], v[68:69], s[12:13] op_sel_hi:[1,0]
	v_pk_fma_f32 v[64:65], v[64:65], v[224:225], v[98:99] op_sel_hi:[1,0,1]
	v_exp_f32_e32 v72, v72
	v_exp_f32_e32 v73, v73
	v_min_f32_e32 v64, 0x40e00000, v64
	v_min_f32_e32 v65, 0x40e00000, v65
	v_pk_mul_f32 v[76:77], v[64:65], s[12:13] op_sel_hi:[1,0]
	v_pk_fma_f32 v[72:73], v[72:73], s[14:15], s[14:15] op_sel_hi:[1,0,0]
	v_exp_f32_e32 v76, v76
	v_rcp_f32_e32 v72, v72
	v_rcp_f32_e32 v73, v73
	v_exp_f32_e32 v77, v77
	v_pk_fma_f32 v[58:59], v[58:59], v[224:225], v[150:151] op_sel_hi:[1,0,1]
	v_pk_fma_f32 v[60:61], v[60:61], v[224:225], v[116:117] op_sel_hi:[1,0,1]
	v_med3_f32 v58, v58, s55, v199
	v_med3_f32 v59, v59, s55, v199
	v_pk_mul_f32 v[68:69], v[68:69], v[72:73]
	v_pk_fma_f32 v[54:55], v[54:55], v[224:225], v[90:91] op_sel_hi:[1,0,1]
	v_pk_mul_f32 v[58:59], v[58:59], v[68:69]
	v_pk_fma_f32 v[68:69], v[76:77], s[14:15], s[14:15] op_sel_hi:[1,0,0]
	v_med3_f32 v60, v60, s55, v199
	v_rcp_f32_e32 v68, v68
	v_rcp_f32_e32 v69, v69
	v_med3_f32 v61, v61, s55, v199
	v_min_f32_e32 v54, 0x40e00000, v54
	v_min_f32_e32 v55, 0x40e00000, v55
	v_pk_mul_f32 v[64:65], v[64:65], v[68:69]
	v_pk_fma_f32 v[56:57], v[56:57], v[224:225], v[74:75] op_sel_hi:[1,0,1]
	v_pk_mul_f32 v[60:61], v[60:61], v[64:65]
	v_pk_mul_f32 v[64:65], v[54:55], s[12:13] op_sel_hi:[1,0]
	v_min_f32_e32 v56, 0x40e00000, v56
	v_exp_f32_e32 v64, v64
	v_exp_f32_e32 v65, v65
	v_min_f32_e32 v57, 0x40e00000, v57
	v_pk_mul_f32 v[68:69], v[56:57], s[12:13] op_sel_hi:[1,0]
	v_pk_fma_f32 v[50:51], v[50:51], v[224:225], v[100:101] op_sel_hi:[1,0,1]
	v_pk_fma_f32 v[64:65], v[64:65], s[14:15], s[14:15] op_sel_hi:[1,0,0]
	v_exp_f32_e32 v68, v68
	v_rcp_f32_e32 v64, v64
	v_rcp_f32_e32 v65, v65
	v_exp_f32_e32 v69, v69
	v_med3_f32 v50, v50, s55, v199
	v_med3_f32 v51, v51, s55, v199
	v_pk_mul_f32 v[54:55], v[54:55], v[64:65]
	s_waitcnt vmcnt(4)
	v_pk_fma_f32 v[46:47], v[46:47], v[226:227], v[114:115] op_sel_hi:[1,0,1]
	v_pk_mul_f32 v[54:55], v[50:51], v[54:55]
	v_pk_mul_f32 v[50:51], v[88:89], v[52:53]
	v_pk_fma_f32 v[52:53], v[68:69], s[14:15], s[14:15] op_sel_hi:[1,0,0]
	v_pk_fma_f32 v[50:51], v[50:51], v[224:225], v[92:93] op_sel_hi:[1,0,1]
	v_rcp_f32_e32 v52, v52
	v_rcp_f32_e32 v53, v53
	v_med3_f32 v50, v50, s55, v199
	v_med3_f32 v51, v51, s55, v199
	v_min_f32_e32 v46, 0x40e00000, v46
	v_pk_mul_f32 v[52:53], v[56:57], v[52:53]
	v_min_f32_e32 v47, 0x40e00000, v47
	v_pk_mul_f32 v[52:53], v[50:51], v[52:53]
	s_nop 0
	v_cvt_pk_fp8_f32 v51, v54, v55
	v_pk_mul_f32 v[54:55], v[46:47], s[12:13] op_sel_hi:[1,0]
	v_pk_fma_f32 v[42:43], v[42:43], v[226:227], v[150:151] op_sel_hi:[1,0,1]
	v_exp_f32_e32 v54, v54
	v_exp_f32_e32 v55, v55
	v_cvt_pk_fp8_f32 v51, v52, v53 op_sel:[0,0,1]
	v_med3_f32 v42, v42, s55, v199
	v_med3_f32 v43, v43, s55, v199
	v_pk_fma_f32 v[52:53], v[54:55], s[14:15], s[14:15] op_sel_hi:[1,0,0]
	v_pk_fma_f32 v[38:39], v[38:39], v[226:227], v[90:91] op_sel_hi:[1,0,1]
	v_rcp_f32_e32 v52, v52
	v_rcp_f32_e32 v53, v53
	v_min_f32_e32 v38, 0x40e00000, v38
	v_min_f32_e32 v39, 0x40e00000, v39
	v_pk_fma_f32 v[44:45], v[44:45], v[226:227], v[116:117] op_sel_hi:[1,0,1]
	v_pk_mul_f32 v[46:47], v[46:47], v[52:53]
	v_pk_mul_f32 v[52:53], v[38:39], s[12:13] op_sel_hi:[1,0]
	v_pk_mul_f32 v[42:43], v[42:43], v[46:47]
	v_pk_mul_f32 v[46:47], v[108:109], v[48:49]
	v_exp_f32_e32 v52, v52
	v_pk_fma_f32 v[46:47], v[46:47], v[226:227], v[98:99] op_sel_hi:[1,0,1]
	v_exp_f32_e32 v53, v53
	v_min_f32_e32 v46, 0x40e00000, v46
	v_min_f32_e32 v47, 0x40e00000, v47
	v_pk_mul_f32 v[48:49], v[46:47], s[12:13] op_sel_hi:[1,0]
	v_med3_f32 v44, v44, s55, v199
	v_exp_f32_e32 v48, v48
	v_exp_f32_e32 v49, v49
	v_med3_f32 v45, v45, s55, v199
	v_pk_fma_f32 v[30:31], v[30:31], v[226:227], v[100:101] op_sel_hi:[1,0,1]
	s_nop 0
	v_pk_fma_f32 v[48:49], v[48:49], s[14:15], s[14:15] op_sel_hi:[1,0,0]
	v_med3_f32 v30, v30, s55, v199
	v_rcp_f32_e32 v48, v48
	v_rcp_f32_e32 v49, v49
	v_med3_f32 v31, v31, s55, v199
	v_cvt_pk_fp8_f32 v50, v58, v59
	v_pk_fma_f32 v[32:33], v[32:33], v[226:227], v[92:93] op_sel_hi:[1,0,1]
	v_pk_mul_f32 v[46:47], v[46:47], v[48:49]
	v_med3_f32 v32, v32, s55, v199
	v_pk_mul_f32 v[44:45], v[44:45], v[46:47]
	v_pk_fma_f32 v[46:47], v[52:53], s[14:15], s[14:15] op_sel_hi:[1,0,0]
	s_nop 0
	v_rcp_f32_e32 v46, v46
	v_rcp_f32_e32 v47, v47
	s_nop 0
	v_cvt_pk_fp8_f32 v52, v42, v43
	v_med3_f32 v33, v33, s55, v199
	v_pk_mul_f32 v[38:39], v[38:39], v[46:47]
	v_cvt_pk_fp8_f32 v50, v60, v61 op_sel:[0,0,1]
	v_pk_mul_f32 v[30:31], v[30:31], v[38:39]
	v_pk_mul_f32 v[38:39], v[84:85], v[40:41]
	v_cvt_pk_fp8_f32 v53, v30, v31
	v_pk_fma_f32 v[38:39], v[38:39], v[226:227], v[74:75] op_sel_hi:[1,0,1]
	v_cvt_pk_fp8_f32 v52, v44, v45 op_sel:[0,0,1]
	v_min_f32_e32 v38, 0x40e00000, v38
	v_min_f32_e32 v39, 0x40e00000, v39
	v_pk_mul_f32 v[40:41], v[38:39], s[12:13] op_sel_hi:[1,0]
	v_permlane16_swap_b32_e32 v50, v52
	v_exp_f32_e32 v40, v40
	v_exp_f32_e32 v41, v41
	s_nop 0
	v_pk_fma_f32 v[40:41], v[40:41], s[14:15], s[14:15] op_sel_hi:[1,0,0]
	s_nop 0
	v_rcp_f32_e32 v40, v40
	v_rcp_f32_e32 v41, v41
	s_nop 0
	v_pk_mul_f32 v[30:31], v[38:39], v[40:41]
	s_nop 0
	v_pk_mul_f32 v[30:31], v[32:33], v[30:31]
	v_cvt_f32_i32_e32 v32, v34
	v_cvt_pk_fp8_f32 v53, v30, v31 op_sel:[0,0,1]
	v_or_b32_e32 v30, v62, v180
	v_ashrrev_i32_e32 v31, 31, v30
	v_lshlrev_b64 v[30:31], 10, v[30:31]
	v_lshl_add_u64 v[30:31], s[94:95], 0, v[30:31]
	v_permlane16_swap_b32_e32 v51, v53
	v_lshl_add_u64 v[30:31], v[30:31], 0, v[146:147]
	global_store_dwordx4 v[30:31], v[50:53], off
	s_nop 0
	v_cvt_f32_i32_e32 v33, v35
	s_nop 0
	v_pk_mul_f32 v[32:33], v[110:111], v[32:33]
	s_waitcnt vmcnt(4)
	v_pk_fma_f32 v[22:23], v[22:23], v[228:229], v[114:115] op_sel_hi:[1,0,1]
	s_nop 0
	v_min_f32_e32 v22, 0x40e00000, v22
	v_min_f32_e32 v23, 0x40e00000, v23
	v_pk_mul_f32 v[38:39], v[22:23], s[12:13] op_sel_hi:[1,0]
	v_pk_fma_f32 v[24:25], v[24:25], v[228:229], v[98:99] op_sel_hi:[1,0,1]
	v_exp_f32_e32 v38, v38
	v_exp_f32_e32 v39, v39
	v_min_f32_e32 v24, 0x40e00000, v24
	v_min_f32_e32 v25, 0x40e00000, v25
	v_pk_mul_f32 v[40:41], v[24:25], s[12:13] op_sel_hi:[1,0]
	v_pk_fma_f32 v[38:39], v[38:39], s[14:15], s[14:15] op_sel_hi:[1,0,0]
	v_exp_f32_e32 v40, v40
	v_rcp_f32_e32 v38, v38
	v_rcp_f32_e32 v39, v39
	v_exp_f32_e32 v41, v41
	v_pk_fma_f32 v[32:33], v[32:33], v[228:229], v[150:151] op_sel_hi:[1,0,1]
	v_pk_fma_f32 v[14:15], v[14:15], v[228:229], v[90:91] op_sel_hi:[1,0,1]
	v_med3_f32 v32, v32, s55, v199
	v_med3_f32 v33, v33, s55, v199
	v_pk_mul_f32 v[22:23], v[22:23], v[38:39]
	v_min_f32_e32 v14, 0x40e00000, v14
	v_pk_mul_f32 v[22:23], v[32:33], v[22:23]
	v_pk_mul_f32 v[32:33], v[112:113], v[36:37]
	v_pk_fma_f32 v[36:37], v[40:41], s[14:15], s[14:15] op_sel_hi:[1,0,0]
	v_pk_fma_f32 v[32:33], v[32:33], v[228:229], v[116:117] op_sel_hi:[1,0,1]
	v_rcp_f32_e32 v36, v36
	v_rcp_f32_e32 v37, v37
	v_med3_f32 v32, v32, s55, v199
	v_med3_f32 v33, v33, s55, v199
	v_min_f32_e32 v15, 0x40e00000, v15
	v_pk_mul_f32 v[24:25], v[24:25], v[36:37]
	v_pk_fma_f32 v[16:17], v[16:17], v[228:229], v[74:75] op_sel_hi:[1,0,1]
	v_pk_mul_f32 v[24:25], v[32:33], v[24:25]
	v_pk_mul_f32 v[32:33], v[14:15], s[12:13] op_sel_hi:[1,0]
	v_min_f32_e32 v16, 0x40e00000, v16
	v_exp_f32_e32 v32, v32
	v_exp_f32_e32 v33, v33
	v_min_f32_e32 v17, 0x40e00000, v17
	v_pk_mul_f32 v[36:37], v[16:17], s[12:13] op_sel_hi:[1,0]
	v_pk_fma_f32 v[26:27], v[26:27], v[228:229], v[100:101] op_sel_hi:[1,0,1]
	v_pk_fma_f32 v[32:33], v[32:33], s[14:15], s[14:15] op_sel_hi:[1,0,0]
	v_exp_f32_e32 v36, v36
	v_rcp_f32_e32 v32, v32
	v_rcp_f32_e32 v33, v33
	v_exp_f32_e32 v37, v37
	v_med3_f32 v26, v26, s55, v199
	v_med3_f32 v27, v27, s55, v199
	v_pk_mul_f32 v[14:15], v[14:15], v[32:33]
	s_waitcnt vmcnt(3)
	v_pk_fma_f32 v[6:7], v[6:7], v[230:231], v[114:115] op_sel_hi:[1,0,1]
	v_pk_mul_f32 v[26:27], v[26:27], v[14:15]
	v_pk_mul_f32 v[14:15], v[88:89], v[28:29]
	v_pk_fma_f32 v[28:29], v[36:37], s[14:15], s[14:15] op_sel_hi:[1,0,0]
	v_pk_fma_f32 v[14:15], v[14:15], v[228:229], v[92:93] op_sel_hi:[1,0,1]
	v_rcp_f32_e32 v28, v28
	v_rcp_f32_e32 v29, v29
	v_med3_f32 v14, v14, s55, v199
	v_med3_f32 v15, v15, s55, v199
	v_min_f32_e32 v6, 0x40e00000, v6
	v_pk_mul_f32 v[16:17], v[16:17], v[28:29]
	v_min_f32_e32 v7, 0x40e00000, v7
	v_pk_mul_f32 v[16:17], v[14:15], v[16:17]
	s_nop 0
	v_cvt_pk_fp8_f32 v14, v22, v23
	s_nop 0
	v_pk_mul_f32 v[22:23], v[6:7], s[12:13] op_sel_hi:[1,0]
	v_cvt_pk_fp8_f32 v15, v26, v27
	v_exp_f32_e32 v22, v22
	v_exp_f32_e32 v23, v23
	v_pk_fma_f32 v[8:9], v[8:9], v[230:231], v[98:99] op_sel_hi:[1,0,1]
	v_cvt_pk_fp8_f32 v15, v16, v17 op_sel:[0,0,1]
	v_pk_mul_f32 v[16:17], v[110:111], v[18:19]
	v_pk_fma_f32 v[18:19], v[22:23], s[14:15], s[14:15] op_sel_hi:[1,0,0]
	v_pk_fma_f32 v[16:17], v[16:17], v[230:231], v[150:151] op_sel_hi:[1,0,1]
	v_rcp_f32_e32 v18, v18
	v_rcp_f32_e32 v19, v19
	v_med3_f32 v16, v16, s55, v199
	v_med3_f32 v17, v17, s55, v199
	v_min_f32_e32 v8, 0x40e00000, v8
	v_pk_mul_f32 v[6:7], v[6:7], v[18:19]
	v_cvt_f32_i32_e32 v19, v21
	v_cvt_f32_i32_e32 v18, v20
	v_min_f32_e32 v9, 0x40e00000, v9
	v_pk_mul_f32 v[6:7], v[16:17], v[6:7]
	v_pk_fma_f32 v[2:3], v[2:3], v[230:231], v[90:91] op_sel_hi:[1,0,1]
	v_pk_mul_f32 v[16:17], v[112:113], v[18:19]
	v_pk_mul_f32 v[18:19], v[8:9], s[12:13] op_sel_hi:[1,0]
	v_min_f32_e32 v2, 0x40e00000, v2
	v_exp_f32_e32 v18, v18
	v_exp_f32_e32 v19, v19
	v_min_f32_e32 v3, 0x40e00000, v3
	v_pk_mul_f32 v[20:21], v[2:3], s[12:13] op_sel_hi:[1,0]
	v_pk_fma_f32 v[16:17], v[16:17], v[230:231], v[116:117] op_sel_hi:[1,0,1]
	v_pk_fma_f32 v[18:19], v[18:19], s[14:15], s[14:15] op_sel_hi:[1,0,0]
	v_exp_f32_e32 v20, v20
	v_rcp_f32_e32 v18, v18
	v_rcp_f32_e32 v19, v19
	v_exp_f32_e32 v21, v21
	v_med3_f32 v16, v16, s55, v199
	v_med3_f32 v17, v17, s55, v199
	v_pk_mul_f32 v[8:9], v[8:9], v[18:19]
	v_pk_fma_f32 v[10:11], v[10:11], v[230:231], v[100:101] op_sel_hi:[1,0,1]
	v_pk_mul_f32 v[8:9], v[16:17], v[8:9]
	v_pk_fma_f32 v[16:17], v[20:21], s[14:15], s[14:15] op_sel_hi:[1,0,0]
	v_pk_fma_f32 v[4:5], v[4:5], v[230:231], v[74:75] op_sel_hi:[1,0,1]
	v_rcp_f32_e32 v16, v16
	v_rcp_f32_e32 v17, v17
	v_med3_f32 v10, v10, s55, v199
	v_med3_f32 v11, v11, s55, v199
	v_min_f32_e32 v4, 0x40e00000, v4
	v_pk_mul_f32 v[2:3], v[2:3], v[16:17]
	v_min_f32_e32 v5, 0x40e00000, v5
	v_pk_mul_f32 v[2:3], v[10:11], v[2:3]
	v_pk_mul_f32 v[10:11], v[88:89], v[12:13]
	v_pk_mul_f32 v[12:13], v[4:5], s[12:13] op_sel_hi:[1,0]
	s_nop 0
	v_exp_f32_e32 v12, v12
	v_exp_f32_e32 v13, v13
	s_nop 0
	v_cvt_pk_fp8_f32 v16, v6, v7
	v_cvt_pk_fp8_f32 v17, v2, v3
	v_pk_fma_f32 v[12:13], v[12:13], s[14:15], s[14:15] op_sel_hi:[1,0,0]
	v_pk_fma_f32 v[10:11], v[10:11], v[230:231], v[92:93] op_sel_hi:[1,0,1]
	v_rcp_f32_e32 v12, v12
	v_rcp_f32_e32 v13, v13
	v_med3_f32 v10, v10, s55, v199
	v_med3_f32 v11, v11, s55, v199
	v_cvt_pk_fp8_f32 v14, v24, v25 op_sel:[0,0,1]
	v_pk_mul_f32 v[2:3], v[4:5], v[12:13]
	v_cvt_pk_fp8_f32 v16, v8, v9 op_sel:[0,0,1]
	v_pk_mul_f32 v[2:3], v[10:11], v[2:3]
	s_nop 0
	v_permlane16_swap_b32_e32 v14, v16
	v_cvt_pk_fp8_f32 v17, v2, v3 op_sel:[0,0,1]
	v_or_b32_e32 v2, v62, v181
	v_ashrrev_i32_e32 v3, 31, v2
	v_lshlrev_b64 v[2:3], 10, v[2:3]
	v_lshl_add_u64 v[2:3], s[94:95], 0, v[2:3]
	v_permlane16_swap_b32_e32 v15, v17
	v_lshl_add_u64 v[2:3], v[2:3], 0, v[146:147]
	global_store_dwordx4 v[2:3], v[14:17], off
	s_cbranch_vccnz .LBB0_3069
	s_andn2_b64 vcc, exec, s[4:5]
	s_cbranch_vccnz .LBB0_3068
	s_barrier
	s_branch .LBB0_3068
